# GEMM K-loops without any s_setprio (on top of saddr-form LDS-DMA, 64B-aligned heads, non-nt epilogue stores, P3/P4/P6/P8 edits): same code as the previous version plus a comment line
# baseline (speedup 1.0000x reference)
; #define PG8_STAGE(bufoff, gbase, voff) do { _Pragma("unroll") for (int _i = 0; _i < 2; ++_i) \
;         __builtin_amdgcn_global_load_lds((const unsigned*)((const char*)(gbase) + (voff)[_i]), (PG8_LAS unsigned*)(lds + (bufoff) + ldsw + _i * 8192), 16, 0, 0); } while (0)
; #define PG8_LDA(dst, b, h) do { _Pragma("unroll") for (int m = 0; m < 4; ++m) _Pragma("unroll") for (int k = 0; k < 2; ++k) dst[m][k] = *(const PG8_LAS bf16x8*)(lds + PG8_SA(b, h) + aoff + m * 2048 + k * 1024); } while (0)
; #define PG8_LDB(dst, b, h) do { _Pragma("unroll") for (int n = 0; n < 2; ++n) _Pragma("unroll") for (int k = 0; k < 2; ++k) dst[n][k] = *(const PG8_LAS bf16x8*)(lds + PG8_SB(b, h) + boff + n * 2048 + k * 1024); } while (0)
; #define PG8_MMA(ai, bj, At, Bt) do { __builtin_amdgcn_s_setprio(1); _Pragma("unroll") for (int m = 0; m < 4; ++m) _Pragma("unroll") for (int n = 0; n < 2; ++n) _Pragma("unroll") for (int k = 0; k < 2; ++k) \
;         acc[ai][bj][m][n] = __builtin_amdgcn_mfma_f32_16x16x32_bf16(Bt[n][k], At[m][k], acc[ai][bj][m][n], 0, 0, 0); __builtin_amdgcn_s_setprio(0); } while (0)
; #define PG8_WAIT_V(n) asm volatile("s_waitcnt vmcnt(" #n ")" ::: "memory")
; #define PG8_WAIT_L(n) asm volatile("s_waitcnt lgkmcnt(" #n ")" ::: "memory")
; template <class Epi, class Sched, bool ALIGN_EPI = false, bool SP2 = false>
; __device__ __forceinline__ void gemm_phase(PG8_LAS unsigned char* lds, const Gemm g, const Sched& S, const Epi& E) {
;     ...
;             const bool last = (t == nt - 2);
;             const char* a1 = cA + (size_t)(t + 1) * kstep;
;             const char* a2 = last ? nA : cA + (size_t)(t + 2) * kstep; const char* b2 = last ? nB : cB + (size_t)(t + 2) * kstep;
;             const char* a3 = a2 + kstep; const char* b3 = b2 + kstep;
;             if (last && has_next) S.a_ready(nxt);
;             if constexpr (SP2) {
;             PG8_LDB(B0, 0, 0); PG8_LDB(B1, 0, 1); PG8_SCHED; PG8_LDA(At, 0, 0); PG8_STAGE(PG8_SA(1, 1), a1 + hstep, voffA);
;             PG8_WAIT_V(8); PG8_WAIT_L(0); PG8_BAR; PG8_MMA(0, 0, At, B0); PG8_MMA(0, 1, At, B1); PG8_BAR; PG8_SCHED;
;             PG8_LDA(At, 0, 1); PG8_STAGE(PG8_SB(0, 0), b2, voffB); PG8_STAGE(PG8_SB(0, 1), b2 + hstep, voffB); PG8_STAGE(PG8_SA(0, 0), a2, voffA);
;             PG8_WAIT_V(8); PG8_WAIT_L(0); PG8_BAR; PG8_MMA(1, 0, At, B0); PG8_MMA(1, 1, At, B1); PG8_BAR; PG8_SCHED;
.LBB0_102:
	ds_read_b128 v[154:157], v159
	ds_read_b128 v[162:165], v159 offset:1024
	ds_read_b128 v[166:169], v159 offset:2048
	ds_read_b128 v[170:173], v159 offset:3072
	ds_read_b128 v[174:177], v160
	ds_read_b128 v[178:181], v160 offset:1024
	ds_read_b128 v[184:187], v160 offset:2048
	ds_read_b128 v[188:191], v160 offset:3072
	s_add_u32 s26, s24, 0xfff00080
	s_addc_u32 s27, s25, -1
	s_cmp_eq_u32 s50, 60
	s_cselect_b32 s29, s17, s27
	s_cselect_b32 s28, s23, s26
	s_cselect_b32 s27, s15, s49
	s_cselect_b32 s26, s46, s47
	s_nop 0
	s_add_i32 m0, s34, 0xc000
	ds_read_b128 v[192:195], v161
	ds_read_b128 v[196:199], v161 offset:1024
	ds_read_b128 v[200:203], v161 offset:2048
	ds_read_b128 v[204:207], v161 offset:3072
	ds_read_b128 v[208:211], v161 offset:4096
	ds_read_b128 v[212:215], v161 offset:5120
	ds_read_b128 v[216:219], v161 offset:6144
	ds_read_b128 v[220:223], v161 offset:7168
	global_load_lds_dwordx4 v146, s[24:25]
	s_nop 0
	s_add_i32 m0, s34, 0xe000
	s_nop 0
	global_load_lds_dwordx4 v148, s[24:25]
	s_waitcnt vmcnt(8)
	s_waitcnt lgkmcnt(0)
	s_barrier
	s_waitcnt lgkmcnt(0)
	v_mfma_f32_16x16x32_bf16 v[126:129], v[154:157], v[192:195], v[126:129]
	v_mfma_f32_16x16x32_bf16 v[122:125], v[166:169], v[192:195], v[122:125]
	v_mfma_f32_16x16x32_bf16 v[110:113], v[154:157], v[200:203], v[110:113]
	v_mfma_f32_16x16x32_bf16 v[106:109], v[166:169], v[200:203], v[106:109]
	v_mfma_f32_16x16x32_bf16 v[98:101], v[154:157], v[208:211], v[98:101]
	v_mfma_f32_16x16x32_bf16 v[90:93], v[166:169], v[208:211], v[90:93]
	v_mfma_f32_16x16x32_bf16 v[82:85], v[154:157], v[216:219], v[82:85]
	v_mfma_f32_16x16x32_bf16 v[74:77], v[166:169], v[216:219], v[74:77]
	v_mfma_f32_16x16x32_bf16 v[126:129], v[162:165], v[196:199], v[126:129]
	v_mfma_f32_16x16x32_bf16 v[122:125], v[170:173], v[196:199], v[122:125]
	v_mfma_f32_16x16x32_bf16 v[110:113], v[162:165], v[204:207], v[110:113]
	v_mfma_f32_16x16x32_bf16 v[106:109], v[170:173], v[204:207], v[106:109]
	v_mfma_f32_16x16x32_bf16 v[98:101], v[162:165], v[212:215], v[98:101]
	v_mfma_f32_16x16x32_bf16 v[90:93], v[170:173], v[212:215], v[90:93]
	v_mfma_f32_16x16x32_bf16 v[82:85], v[162:165], v[220:223], v[82:85]
	v_mfma_f32_16x16x32_bf16 v[74:77], v[170:173], v[220:223], v[74:77]
	v_mfma_f32_16x16x32_bf16 v[118:121], v[174:177], v[192:195], v[118:121]
	v_mfma_f32_16x16x32_bf16 v[114:117], v[184:187], v[192:195], v[114:117]
	v_mfma_f32_16x16x32_bf16 v[102:105], v[174:177], v[200:203], v[102:105]
	v_mfma_f32_16x16x32_bf16 v[94:97], v[184:187], v[200:203], v[94:97]
	v_mfma_f32_16x16x32_bf16 v[86:89], v[174:177], v[208:211], v[86:89]
	v_mfma_f32_16x16x32_bf16 v[78:81], v[184:187], v[208:211], v[78:81]
	v_mfma_f32_16x16x32_bf16 v[70:73], v[174:177], v[216:219], v[70:73]
	v_mfma_f32_16x16x32_bf16 v[66:69], v[184:187], v[216:219], v[66:69]
	v_mfma_f32_16x16x32_bf16 v[118:121], v[178:181], v[196:199], v[118:121]
	v_mfma_f32_16x16x32_bf16 v[114:117], v[188:191], v[196:199], v[114:117]
	v_mfma_f32_16x16x32_bf16 v[102:105], v[178:181], v[204:207], v[102:105]
	v_mfma_f32_16x16x32_bf16 v[94:97], v[188:191], v[204:207], v[94:97]
	v_mfma_f32_16x16x32_bf16 v[86:89], v[178:181], v[212:215], v[86:89]
	v_mfma_f32_16x16x32_bf16 v[78:81], v[188:191], v[212:215], v[78:81]
	v_mfma_f32_16x16x32_bf16 v[70:73], v[178:181], v[220:223], v[70:73]
	v_mfma_f32_16x16x32_bf16 v[66:69], v[188:191], v[220:223], v[66:69]
	s_barrier
	s_add_i32 s51, s42, s30
	s_nop 0
	s_mov_b32 m0, s51
	ds_read_b128 v[192:195], v161 offset:16384
	ds_read_b128 v[196:199], v161 offset:17408
	ds_read_b128 v[200:203], v161 offset:18432
	ds_read_b128 v[204:207], v161 offset:19456
	ds_read_b128 v[208:211], v161 offset:20480
	ds_read_b128 v[212:215], v161 offset:21504
	ds_read_b128 v[216:219], v161 offset:22528
	ds_read_b128 v[220:223], v161 offset:23552
	global_load_lds_dwordx4 v140, s[26:27]
	s_add_i32 m0, s51, 0x2000
	s_add_u32 s52, s26, 0x100000
	s_nop 0
	s_addc_u32 s53, s27, 0
	s_add_i32 s51, s43, s30
	global_load_lds_dwordx4 v136, s[26:27]
	s_nop 0
	s_mov_b32 m0, s51
	s_add_u32 s58, s28, s6
	s_addc_u32 s59, s29, s7
	global_load_lds_dwordx4 v140, s[52:53]
	s_nop 0
	s_add_i32 m0, s51, 0x2000
	s_nop 0
	global_load_lds_dwordx4 v136, s[52:53]
	s_nop 0
	s_mov_b32 m0, s34
	s_nop 0
	global_load_lds_dwordx4 v142, s[28:29]
	s_mov_b32 m0, s35
	s_nop 0
	global_load_lds_dwordx4 v138, s[28:29]
	s_waitcnt vmcnt(8)
	s_waitcnt lgkmcnt(0)
	s_barrier
	s_waitcnt lgkmcnt(0)
	v_mfma_f32_16x16x32_bf16 v[62:65], v[154:157], v[192:195], v[62:65]
	v_mfma_f32_16x16x32_bf16 v[58:61], v[166:169], v[192:195], v[58:61]
	v_mfma_f32_16x16x32_bf16 v[50:53], v[154:157], v[200:203], v[50:53]
	v_mfma_f32_16x16x32_bf16 v[42:45], v[166:169], v[200:203], v[42:45]
	v_mfma_f32_16x16x32_bf16 v[34:37], v[154:157], v[208:211], v[34:37]
	v_mfma_f32_16x16x32_bf16 v[26:29], v[166:169], v[208:211], v[26:29]
	v_mfma_f32_16x16x32_bf16 v[18:21], v[154:157], v[216:219], v[18:21]
	v_mfma_f32_16x16x32_bf16 v[10:13], v[166:169], v[216:219], v[10:13]
	v_mfma_f32_16x16x32_bf16 v[62:65], v[162:165], v[196:199], v[62:65]
	v_mfma_f32_16x16x32_bf16 v[58:61], v[170:173], v[196:199], v[58:61]
	v_mfma_f32_16x16x32_bf16 v[50:53], v[162:165], v[204:207], v[50:53]
	v_mfma_f32_16x16x32_bf16 v[42:45], v[170:173], v[204:207], v[42:45]
	v_mfma_f32_16x16x32_bf16 v[34:37], v[162:165], v[212:215], v[34:37]
	v_mfma_f32_16x16x32_bf16 v[26:29], v[170:173], v[212:215], v[26:29]
	v_mfma_f32_16x16x32_bf16 v[18:21], v[162:165], v[220:223], v[18:21]
	v_mfma_f32_16x16x32_bf16 v[10:13], v[170:173], v[220:223], v[10:13]
	v_mfma_f32_16x16x32_bf16 v[54:57], v[174:177], v[192:195], v[54:57]
	v_mfma_f32_16x16x32_bf16 v[46:49], v[184:187], v[192:195], v[46:49]
	v_mfma_f32_16x16x32_bf16 v[38:41], v[174:177], v[200:203], v[38:41]
	v_mfma_f32_16x16x32_bf16 v[30:33], v[184:187], v[200:203], v[30:33]
	v_mfma_f32_16x16x32_bf16 v[22:25], v[174:177], v[208:211], v[22:25]
	v_mfma_f32_16x16x32_bf16 v[14:17], v[184:187], v[208:211], v[14:17]
	v_mfma_f32_16x16x32_bf16 v[6:9], v[174:177], v[216:219], v[6:9]
	v_mfma_f32_16x16x32_bf16 v[2:5], v[184:187], v[216:219], v[2:5]
	v_mfma_f32_16x16x32_bf16 v[54:57], v[178:181], v[196:199], v[54:57]
	v_mfma_f32_16x16x32_bf16 v[46:49], v[188:191], v[196:199], v[46:49]
	v_mfma_f32_16x16x32_bf16 v[38:41], v[178:181], v[204:207], v[38:41]
	v_mfma_f32_16x16x32_bf16 v[30:33], v[188:191], v[204:207], v[30:33]
	v_mfma_f32_16x16x32_bf16 v[22:25], v[178:181], v[212:215], v[22:25]
	v_mfma_f32_16x16x32_bf16 v[14:17], v[188:191], v[212:215], v[14:17]
	v_mfma_f32_16x16x32_bf16 v[6:9], v[178:181], v[220:223], v[6:9]
	v_mfma_f32_16x16x32_bf16 v[2:5], v[188:191], v[220:223], v[2:5]
	s_barrier
; #define PG8_STAGE(bufoff, gbase, voff) do { _Pragma("unroll") for (int _i = 0; _i < 2; ++_i) \
;         __builtin_amdgcn_global_load_lds((const unsigned*)((const char*)(gbase) + (voff)[_i]), (PG8_LAS unsigned*)(lds + (bufoff) + ldsw + _i * 8192), 16, 0, 0); } while (0)
; #define PG8_LDA(dst, b, h) do { _Pragma("unroll") for (int m = 0; m < 4; ++m) _Pragma("unroll") for (int k = 0; k < 2; ++k) dst[m][k] = *(const PG8_LAS bf16x8*)(lds + PG8_SA(b, h) + aoff + m * 2048 + k * 1024); } while (0)
; #define PG8_LDB(dst, b, h) do { _Pragma("unroll") for (int n = 0; n < 2; ++n) _Pragma("unroll") for (int k = 0; k < 2; ++k) dst[n][k] = *(const PG8_LAS bf16x8*)(lds + PG8_SB(b, h) + boff + n * 2048 + k * 1024); } while (0)
; #define PG8_MMA(ai, bj, At, Bt) do { __builtin_amdgcn_s_setprio(1); _Pragma("unroll") for (int m = 0; m < 4; ++m) _Pragma("unroll") for (int n = 0; n < 2; ++n) _Pragma("unroll") for (int k = 0; k < 2; ++k) \
;         acc[ai][bj][m][n] = __builtin_amdgcn_mfma_f32_16x16x32_bf16(Bt[n][k], At[m][k], acc[ai][bj][m][n], 0, 0, 0); __builtin_amdgcn_s_setprio(0); } while (0)
; #define PG8_WAIT_V(n) asm volatile("s_waitcnt vmcnt(" #n ")" ::: "memory")
; #define PG8_WAIT_L(n) asm volatile("s_waitcnt lgkmcnt(" #n ")" ::: "memory")
; #define PG8_BAR __builtin_amdgcn_s_barrier()
; #define PG8_SCHED __builtin_amdgcn_sched_barrier(0)
; template <class Epi, class Sched, bool ALIGN_EPI = false, bool SP2 = false>
; __device__ __forceinline__ void gemm_phase(PG8_LAS unsigned char* lds, const Gemm g, const Sched& S, const Epi& E) {
;     ...
;             PG8_LDB(B0, 1, 0); PG8_LDB(B1, 1, 1); PG8_SCHED; PG8_LDA(At, 1, 0); PG8_STAGE(PG8_SA(0, 1), a2 + hstep, voffA);
;             PG8_WAIT_V(8); PG8_WAIT_L(0); PG8_BAR; PG8_MMA(0, 0, At, B0); PG8_MMA(0, 1, At, B1); PG8_BAR; PG8_SCHED;
;             PG8_LDA(At, 1, 1); PG8_STAGE(PG8_SB(1, 0), b3, voffB); PG8_STAGE(PG8_SB(1, 1), b3 + hstep, voffB); PG8_STAGE(PG8_SA(1, 0), a3, voffA);
;             PG8_WAIT_V(8); PG8_WAIT_L(0); PG8_BAR; PG8_MMA(1, 0, At, B0); PG8_MMA(1, 1, At, B1); PG8_BAR; PG8_SCHED;
	s_add_i32 s51, 0, 0x18000
	v_add_u32_e32 v144, s51, v133
	s_add_i32 s52, 0, 0x1c000
	ds_read_b128 v[154:157], v144
	ds_read_b128 v[162:165], v144 offset:1024
	ds_read_b128 v[166:169], v144 offset:2048
	ds_read_b128 v[170:173], v144 offset:3072
	v_add_u32_e32 v144, s52, v133
	ds_read_b128 v[174:177], v144
	ds_read_b128 v[178:181], v144 offset:1024
	ds_read_b128 v[184:187], v144 offset:2048
	ds_read_b128 v[188:191], v144 offset:3072
	s_add_u32 s28, s28, 0x100000
	s_addc_u32 s29, s29, 0
	s_mov_b32 m0, s36
	s_nop 0
	ds_read_b128 v[192:195], v161 offset:32768
	ds_read_b128 v[196:199], v161 offset:33792
	ds_read_b128 v[200:203], v161 offset:34816
	ds_read_b128 v[204:207], v161 offset:35840
	ds_read_b128 v[208:211], v161 offset:36864
	ds_read_b128 v[212:215], v161 offset:37888
	ds_read_b128 v[216:219], v161 offset:38912
	ds_read_b128 v[220:223], v161 offset:39936
	global_load_lds_dwordx4 v142, s[28:29]
	s_nop 0
	s_mov_b32 m0, s37
	s_nop 0
	global_load_lds_dwordx4 v138, s[28:29]
	s_waitcnt vmcnt(8)
	s_waitcnt lgkmcnt(0)
	s_barrier
	s_waitcnt lgkmcnt(0)
	v_mfma_f32_16x16x32_bf16 v[126:129], v[154:157], v[192:195], v[126:129]
	v_mfma_f32_16x16x32_bf16 v[122:125], v[166:169], v[192:195], v[122:125]
	v_mfma_f32_16x16x32_bf16 v[110:113], v[154:157], v[200:203], v[110:113]
	v_mfma_f32_16x16x32_bf16 v[106:109], v[166:169], v[200:203], v[106:109]
	v_mfma_f32_16x16x32_bf16 v[98:101], v[154:157], v[208:211], v[98:101]
	v_mfma_f32_16x16x32_bf16 v[90:93], v[166:169], v[208:211], v[90:93]
	v_mfma_f32_16x16x32_bf16 v[82:85], v[154:157], v[216:219], v[82:85]
	v_mfma_f32_16x16x32_bf16 v[74:77], v[166:169], v[216:219], v[74:77]
	v_mfma_f32_16x16x32_bf16 v[126:129], v[162:165], v[196:199], v[126:129]
	v_mfma_f32_16x16x32_bf16 v[122:125], v[170:173], v[196:199], v[122:125]
	v_mfma_f32_16x16x32_bf16 v[110:113], v[162:165], v[204:207], v[110:113]
	v_mfma_f32_16x16x32_bf16 v[106:109], v[170:173], v[204:207], v[106:109]
	v_mfma_f32_16x16x32_bf16 v[98:101], v[162:165], v[212:215], v[98:101]
	v_mfma_f32_16x16x32_bf16 v[90:93], v[170:173], v[212:215], v[90:93]
	v_mfma_f32_16x16x32_bf16 v[82:85], v[162:165], v[220:223], v[82:85]
	v_mfma_f32_16x16x32_bf16 v[74:77], v[170:173], v[220:223], v[74:77]
	v_mfma_f32_16x16x32_bf16 v[118:121], v[174:177], v[192:195], v[118:121]
	v_mfma_f32_16x16x32_bf16 v[114:117], v[184:187], v[192:195], v[114:117]
	v_mfma_f32_16x16x32_bf16 v[102:105], v[174:177], v[200:203], v[102:105]
	v_mfma_f32_16x16x32_bf16 v[94:97], v[184:187], v[200:203], v[94:97]
	v_mfma_f32_16x16x32_bf16 v[86:89], v[174:177], v[208:211], v[86:89]
	v_mfma_f32_16x16x32_bf16 v[78:81], v[184:187], v[208:211], v[78:81]
	v_mfma_f32_16x16x32_bf16 v[70:73], v[174:177], v[216:219], v[70:73]
	v_mfma_f32_16x16x32_bf16 v[66:69], v[184:187], v[216:219], v[66:69]
	v_mfma_f32_16x16x32_bf16 v[118:121], v[178:181], v[196:199], v[118:121]
	v_mfma_f32_16x16x32_bf16 v[114:117], v[188:191], v[196:199], v[114:117]
	v_mfma_f32_16x16x32_bf16 v[102:105], v[178:181], v[204:207], v[102:105]
	v_mfma_f32_16x16x32_bf16 v[94:97], v[188:191], v[204:207], v[94:97]
	v_mfma_f32_16x16x32_bf16 v[86:89], v[178:181], v[212:215], v[86:89]
	v_mfma_f32_16x16x32_bf16 v[78:81], v[188:191], v[212:215], v[78:81]
	v_mfma_f32_16x16x32_bf16 v[70:73], v[178:181], v[220:223], v[70:73]
	v_mfma_f32_16x16x32_bf16 v[66:69], v[188:191], v[220:223], v[66:69]
	s_barrier
	s_add_i32 s28, s51, s30
	s_add_u32 s54, s26, s6
	s_addc_u32 s55, s27, s7
	s_mov_b32 m0, s28
	ds_read_b128 v[192:195], v161 offset:49152
	ds_read_b128 v[196:199], v161 offset:50176
	ds_read_b128 v[200:203], v161 offset:51200
	ds_read_b128 v[204:207], v161 offset:52224
	ds_read_b128 v[208:211], v161 offset:53248
	ds_read_b128 v[212:215], v161 offset:54272
	ds_read_b128 v[216:219], v161 offset:55296
	ds_read_b128 v[220:223], v161 offset:56320
	global_load_lds_dwordx4 v140, s[54:55]
	s_add_i32 m0, s28, 0x2000
	s_add_u32 s26, s26, 0x100080
	s_nop 0
	s_addc_u32 s27, s27, 0
	s_add_i32 s28, s52, s30
	global_load_lds_dwordx4 v136, s[54:55]
	s_nop 0
	s_mov_b32 m0, s28
	s_nop 0
	global_load_lds_dwordx4 v140, s[26:27]
	s_nop 0
	s_add_i32 m0, s28, 0x2000
	s_nop 0
	global_load_lds_dwordx4 v136, s[26:27]
	s_nop 0
	s_mov_b32 m0, s39
	s_nop 0
	global_load_lds_dwordx4 v142, s[58:59]
	s_nop 0
	s_mov_b32 m0, s40
	s_nop 0
	global_load_lds_dwordx4 v138, s[58:59]
	s_waitcnt vmcnt(8)
	s_waitcnt lgkmcnt(0)
	s_barrier
	s_waitcnt lgkmcnt(0)
	v_mfma_f32_16x16x32_bf16 v[62:65], v[154:157], v[192:195], v[62:65]
	v_mfma_f32_16x16x32_bf16 v[58:61], v[166:169], v[192:195], v[58:61]
	v_mfma_f32_16x16x32_bf16 v[50:53], v[154:157], v[200:203], v[50:53]
	v_mfma_f32_16x16x32_bf16 v[42:45], v[166:169], v[200:203], v[42:45]
	v_mfma_f32_16x16x32_bf16 v[34:37], v[154:157], v[208:211], v[34:37]
	v_mfma_f32_16x16x32_bf16 v[26:29], v[166:169], v[208:211], v[26:29]
	v_mfma_f32_16x16x32_bf16 v[18:21], v[154:157], v[216:219], v[18:21]
	v_mfma_f32_16x16x32_bf16 v[10:13], v[166:169], v[216:219], v[10:13]
	v_mfma_f32_16x16x32_bf16 v[62:65], v[162:165], v[196:199], v[62:65]
	v_mfma_f32_16x16x32_bf16 v[58:61], v[170:173], v[196:199], v[58:61]
	v_mfma_f32_16x16x32_bf16 v[50:53], v[162:165], v[204:207], v[50:53]
	v_mfma_f32_16x16x32_bf16 v[42:45], v[170:173], v[204:207], v[42:45]
	v_mfma_f32_16x16x32_bf16 v[34:37], v[162:165], v[212:215], v[34:37]
	v_mfma_f32_16x16x32_bf16 v[26:29], v[170:173], v[212:215], v[26:29]
	v_mfma_f32_16x16x32_bf16 v[18:21], v[162:165], v[220:223], v[18:21]
	v_mfma_f32_16x16x32_bf16 v[10:13], v[170:173], v[220:223], v[10:13]
	v_mfma_f32_16x16x32_bf16 v[54:57], v[174:177], v[192:195], v[54:57]
	v_mfma_f32_16x16x32_bf16 v[46:49], v[184:187], v[192:195], v[46:49]
	v_mfma_f32_16x16x32_bf16 v[38:41], v[174:177], v[200:203], v[38:41]
	v_mfma_f32_16x16x32_bf16 v[30:33], v[184:187], v[200:203], v[30:33]
	v_mfma_f32_16x16x32_bf16 v[22:25], v[174:177], v[208:211], v[22:25]
	v_mfma_f32_16x16x32_bf16 v[14:17], v[184:187], v[208:211], v[14:17]
	v_mfma_f32_16x16x32_bf16 v[6:9], v[174:177], v[216:219], v[6:9]
	v_mfma_f32_16x16x32_bf16 v[2:5], v[184:187], v[216:219], v[2:5]
	v_mfma_f32_16x16x32_bf16 v[54:57], v[178:181], v[196:199], v[54:57]
	v_mfma_f32_16x16x32_bf16 v[46:49], v[188:191], v[196:199], v[46:49]
	v_mfma_f32_16x16x32_bf16 v[38:41], v[178:181], v[204:207], v[38:41]
	v_mfma_f32_16x16x32_bf16 v[30:33], v[188:191], v[204:207], v[30:33]
	v_mfma_f32_16x16x32_bf16 v[22:25], v[178:181], v[212:215], v[22:25]
	v_mfma_f32_16x16x32_bf16 v[14:17], v[188:191], v[212:215], v[14:17]
	v_mfma_f32_16x16x32_bf16 v[6:9], v[178:181], v[220:223], v[6:9]
	v_mfma_f32_16x16x32_bf16 v[2:5], v[188:191], v[220:223], v[2:5]
	s_barrier
	s_add_i32 s50, s50, 2
	s_add_u32 s24, s24, 0x100
	s_addc_u32 s25, s25, 0
	s_add_u32 s47, s47, 0x100
	s_addc_u32 s49, s49, 0
	s_cmp_gt_u32 s50, 61
	s_cbranch_scc0 .LBB0_102
	s_and_b64 vcc, exec, s[12:13]
	s_cbranch_vccz .LBB0_105
	s_barrier

; #define PG8_STAGE(bufoff, gbase, voff) do { _Pragma("unroll") for (int _i = 0; _i < 2; ++_i) \
;         __builtin_amdgcn_global_load_lds((const unsigned*)((const char*)(gbase) + (voff)[_i]), (PG8_LAS unsigned*)(lds + (bufoff) + ldsw + _i * 8192), 16, 0, 0); } while (0)
; #define PG8_LDA(dst, b, h) do { _Pragma("unroll") for (int m = 0; m < 4; ++m) _Pragma("unroll") for (int k = 0; k < 2; ++k) dst[m][k] = *(const PG8_LAS bf16x8*)(lds + PG8_SA(b, h) + aoff + m * 2048 + k * 1024); } while (0)
; #define PG8_LDB(dst, b, h) do { _Pragma("unroll") for (int n = 0; n < 2; ++n) _Pragma("unroll") for (int k = 0; k < 2; ++k) dst[n][k] = *(const PG8_LAS bf16x8*)(lds + PG8_SB(b, h) + boff + n * 2048 + k * 1024); } while (0)
; #define PG8_WAIT_V(n) asm volatile("s_waitcnt vmcnt(" #n ")" ::: "memory")
; #define PG8_WAIT_L(n) asm volatile("s_waitcnt lgkmcnt(" #n ")" ::: "memory")
; #define PG8_BAR __builtin_amdgcn_s_barrier()
; #define PG8_SCHED __builtin_amdgcn_sched_barrier(0)
; template <class Epi, class Sched, bool ALIGN_EPI = false, bool SP2 = false>
; __device__ __forceinline__ void gemm_phase(PG8_LAS unsigned char* lds, const Gemm g, const Sched& S, const Epi& E) {
;     ...
;         const char* nA = has_next ? (const char*)g.A + (size_t)nxt.pm * tstep : cA; const char* nB = has_next ? (const char*)g.Bt + (size_t)nxt.pn * tstep : cB;
;         for (int t = 0; t < nt; t += 2) {
;             const bool last = (t == nt - 2);
;             const char* a1 = cA + (size_t)(t + 1) * kstep;
;             const char* a2 = last ? nA : cA + (size_t)(t + 2) * kstep; const char* b2 = last ? nB : cB + (size_t)(t + 2) * kstep;
;             const char* a3 = a2 + kstep; const char* b3 = b2 + kstep;
;             if (last && has_next) S.a_ready(nxt);
;             if constexpr (SP2) {
;             PG8_LDB(B0, 0, 0); PG8_LDB(B1, 0, 1); PG8_SCHED; PG8_LDA(At, 0, 0); PG8_STAGE(PG8_SA(1, 1), a1 + hstep, voffA);
;             PG8_WAIT_V(8); PG8_WAIT_L(0); PG8_BAR; PG8_MMA(0, 0, At, B0); PG8_MMA(0, 1, At, B1); PG8_BAR; PG8_SCHED;
;     ...
; #pragma unroll
;         for (int a = 0; a < 2; ++a)
; #pragma unroll
;             for (int b = 0; b < 2; ++b)
; #pragma unroll
;                 for (int m = 0; m < 4; ++m)
; #pragma unroll
;                     for (int n = 0; n < 2; ++n) acc[a][b][m][n] = (f32x4){0.f, 0.f, 0.f, 0.f};
;         cur = nxt; cA = nA; cB = nB; ++ui;
.LBB0_562:
	s_ashr_i32 s21, s20, 31
	s_lshl_b64 s[22:23], s[20:21], 22
	s_add_u32 s22, s64, s22
	s_addc_u32 s23, s65, s23
	s_and_b64 s[24:25], s[4:5], exec
	s_cselect_b32 s21, s23, s29
	s_cselect_b32 s47, s22, s28
	s_ashr_i32 s19, s18, 31
	s_lshl_b64 s[24:25], s[18:19], 22
	s_add_u32 s24, s56, s24
	s_addc_u32 s25, s57, s25
	s_and_b64 s[34:35], s[4:5], exec
	s_cselect_b32 s19, s25, s31
	s_cselect_b32 s48, s24, s30
	s_add_u32 s28, s28, 0x200080
	s_addc_u32 s29, s29, 0
	s_add_u32 s49, s30, 0x100
	v_mov_b32_e32 v2, 0
	s_addc_u32 s50, s31, 0
	s_mov_b32 s51, -2
	v_mov_b32_e32 v3, v2
	v_mov_b32_e32 v4, v2
	v_mov_b32_e32 v5, v2
	v_mov_b32_e32 v6, v2
	v_mov_b32_e32 v7, v2
	v_mov_b32_e32 v8, v2
	v_mov_b32_e32 v9, v2
	v_mov_b32_e32 v18, v2
	v_mov_b32_e32 v19, v2
	v_mov_b32_e32 v20, v2
	v_mov_b32_e32 v21, v2
	v_mov_b32_e32 v22, v2
	v_mov_b32_e32 v23, v2
	v_mov_b32_e32 v24, v2
	v_mov_b32_e32 v25, v2
	v_mov_b32_e32 v34, v2
	v_mov_b32_e32 v35, v2
	v_mov_b32_e32 v36, v2
	v_mov_b32_e32 v37, v2
	v_mov_b32_e32 v38, v2
	v_mov_b32_e32 v39, v2
	v_mov_b32_e32 v40, v2
	v_mov_b32_e32 v41, v2
	v_mov_b32_e32 v50, v2
	v_mov_b32_e32 v51, v2
	v_mov_b32_e32 v52, v2
	v_mov_b32_e32 v53, v2
	v_mov_b32_e32 v54, v2
	v_mov_b32_e32 v55, v2
	v_mov_b32_e32 v56, v2
	v_mov_b32_e32 v57, v2
	v_mov_b32_e32 v10, v2
	v_mov_b32_e32 v11, v2
	v_mov_b32_e32 v12, v2
	v_mov_b32_e32 v13, v2
	v_mov_b32_e32 v14, v2
	v_mov_b32_e32 v15, v2
	v_mov_b32_e32 v16, v2
	v_mov_b32_e32 v17, v2
	v_mov_b32_e32 v26, v2
	v_mov_b32_e32 v27, v2
	v_mov_b32_e32 v28, v2
	v_mov_b32_e32 v29, v2
	v_mov_b32_e32 v30, v2
	v_mov_b32_e32 v31, v2
	v_mov_b32_e32 v32, v2
	v_mov_b32_e32 v33, v2
	v_mov_b32_e32 v42, v2
	v_mov_b32_e32 v43, v2
	v_mov_b32_e32 v44, v2
	v_mov_b32_e32 v45, v2
	v_mov_b32_e32 v46, v2
	v_mov_b32_e32 v47, v2
	v_mov_b32_e32 v48, v2
	v_mov_b32_e32 v49, v2
	v_mov_b32_e32 v58, v2
	v_mov_b32_e32 v59, v2
	v_mov_b32_e32 v60, v2
	v_mov_b32_e32 v61, v2
	v_mov_b32_e32 v62, v2
	v_mov_b32_e32 v63, v2
	v_mov_b32_e32 v64, v2
	v_mov_b32_e32 v65, v2
	s_waitcnt vmcnt(0)
	v_mov_b32_e32 v66, v2
	v_mov_b32_e32 v67, v2
	v_mov_b32_e32 v68, v2
	v_mov_b32_e32 v69, v2
	v_mov_b32_e32 v70, v2
	v_mov_b32_e32 v71, v2
	v_mov_b32_e32 v72, v2
	v_mov_b32_e32 v73, v2
	v_mov_b32_e32 v82, v2
	v_mov_b32_e32 v83, v2
	v_mov_b32_e32 v84, v2
	v_mov_b32_e32 v85, v2
	v_mov_b32_e32 v86, v2
	v_mov_b32_e32 v87, v2
	v_mov_b32_e32 v88, v2
	v_mov_b32_e32 v89, v2
	v_mov_b32_e32 v98, v2
	v_mov_b32_e32 v99, v2
	v_mov_b32_e32 v100, v2
	v_mov_b32_e32 v101, v2
	v_mov_b32_e32 v102, v2
	v_mov_b32_e32 v103, v2
	v_mov_b32_e32 v104, v2
	v_mov_b32_e32 v105, v2
	v_mov_b32_e32 v114, v2
	v_mov_b32_e32 v115, v2
	v_mov_b32_e32 v116, v2
	v_mov_b32_e32 v117, v2
	v_mov_b32_e32 v118, v2
	v_mov_b32_e32 v119, v2
	v_mov_b32_e32 v120, v2
	v_mov_b32_e32 v121, v2
	v_mov_b32_e32 v74, v2
	v_mov_b32_e32 v75, v2
	v_mov_b32_e32 v76, v2
	v_mov_b32_e32 v77, v2
	v_mov_b32_e32 v78, v2
	v_mov_b32_e32 v79, v2
	v_mov_b32_e32 v80, v2
	v_mov_b32_e32 v81, v2
	v_mov_b32_e32 v90, v2
	v_mov_b32_e32 v91, v2
	v_mov_b32_e32 v92, v2
	v_mov_b32_e32 v93, v2
	v_mov_b32_e32 v94, v2
	v_mov_b32_e32 v95, v2
	v_mov_b32_e32 v96, v2
	v_mov_b32_e32 v97, v2
	v_mov_b32_e32 v106, v2
	v_mov_b32_e32 v107, v2
	v_mov_b32_e32 v108, v2
	v_mov_b32_e32 v109, v2
	v_mov_b32_e32 v110, v2
	v_mov_b32_e32 v111, v2
	v_mov_b32_e32 v112, v2
	v_mov_b32_e32 v113, v2
	v_mov_b32_e32 v122, v2
	v_mov_b32_e32 v123, v2
	v_mov_b32_e32 v124, v2
	v_mov_b32_e32 v125, v2
	v_mov_b32_e32 v126, v2
	v_mov_b32_e32 v127, v2
	v_mov_b32_e32 v128, v2
	v_mov_b32_e32 v129, v2
	s_nop 0
	s_nop 0
	s_nop 0
	s_nop 0
	s_nop 0
	s_nop 0
	s_nop 0
	s_nop 0
	s_nop 0
	s_nop 0
	s_nop 0
	s_nop 0
	s_nop 0
	s_nop 0
	s_nop 0
	s_nop 0
	s_nop 0
.LBB0_563:
	ds_read_b128 v[146:149], v154
	ds_read_b128 v[158:161], v154 offset:1024
	ds_read_b128 v[162:165], v154 offset:2048
	ds_read_b128 v[166:169], v154 offset:3072
	ds_read_b128 v[170:173], v155
	ds_read_b128 v[174:177], v155 offset:1024
	ds_read_b128 v[178:181], v155 offset:2048
	ds_read_b128 v[184:187], v155 offset:3072
	s_add_u32 s30, s28, 0xffe00080
	s_addc_u32 s31, s29, -1
	s_cmpk_eq_i32 s51, 0x7c
	s_cselect_b32 s35, s21, s31
	s_cselect_b32 s34, s47, s30
	s_cselect_b32 s31, s19, s50
	s_cselect_b32 s30, s48, s49
	s_nop 0
	s_add_i32 m0, s27, 0xc000
	ds_read_b128 v[188:191], v156
	ds_read_b128 v[192:195], v156 offset:1024
	ds_read_b128 v[196:199], v156 offset:2048
	ds_read_b128 v[200:203], v156 offset:3072
	ds_read_b128 v[204:207], v156 offset:4096
	ds_read_b128 v[208:211], v156 offset:5120
	ds_read_b128 v[212:215], v156 offset:6144
	ds_read_b128 v[216:219], v156 offset:7168
	global_load_lds_dwordx4 v138, s[28:29]
	s_nop 0
	s_add_i32 m0, s27, 0xe000
	s_nop 0
	global_load_lds_dwordx4 v140, s[28:29]
	s_waitcnt vmcnt(8)
	s_waitcnt lgkmcnt(0)
	s_barrier
; #define PG8_STAGE(bufoff, gbase, voff) do { _Pragma("unroll") for (int _i = 0; _i < 2; ++_i) \
;         __builtin_amdgcn_global_load_lds((const unsigned*)((const char*)(gbase) + (voff)[_i]), (PG8_LAS unsigned*)(lds + (bufoff) + ldsw + _i * 8192), 16, 0, 0); } while (0)
; #define PG8_LDA(dst, b, h) do { _Pragma("unroll") for (int m = 0; m < 4; ++m) _Pragma("unroll") for (int k = 0; k < 2; ++k) dst[m][k] = *(const PG8_LAS bf16x8*)(lds + PG8_SA(b, h) + aoff + m * 2048 + k * 1024); } while (0)
; #define PG8_MMA(ai, bj, At, Bt) do { __builtin_amdgcn_s_setprio(1); _Pragma("unroll") for (int m = 0; m < 4; ++m) _Pragma("unroll") for (int n = 0; n < 2; ++n) _Pragma("unroll") for (int k = 0; k < 2; ++k) \
;         acc[ai][bj][m][n] = __builtin_amdgcn_mfma_f32_16x16x32_bf16(Bt[n][k], At[m][k], acc[ai][bj][m][n], 0, 0, 0); __builtin_amdgcn_s_setprio(0); } while (0)
; #define PG8_WAIT_V(n) asm volatile("s_waitcnt vmcnt(" #n ")" ::: "memory")
; #define PG8_WAIT_L(n) asm volatile("s_waitcnt lgkmcnt(" #n ")" ::: "memory")
; #define PG8_BAR __builtin_amdgcn_s_barrier()
; #define PG8_SCHED __builtin_amdgcn_sched_barrier(0)
; template <class Epi, class Sched, bool ALIGN_EPI = false, bool SP2 = false>
; __device__ __forceinline__ void gemm_phase(PG8_LAS unsigned char* lds, const Gemm g, const Sched& S, const Epi& E) {
;     ...
;             PG8_WAIT_V(8); PG8_WAIT_L(0); PG8_BAR; PG8_MMA(0, 0, At, B0); PG8_MMA(0, 1, At, B1); PG8_BAR; PG8_SCHED;
;             PG8_LDA(At, 0, 1); PG8_STAGE(PG8_SB(0, 0), b2, voffB); PG8_STAGE(PG8_SB(0, 1), b2 + hstep, voffB); PG8_STAGE(PG8_SA(0, 0), a2, voffA);
;             PG8_WAIT_V(8); PG8_WAIT_L(0); PG8_BAR; PG8_MMA(1, 0, At, B0); PG8_MMA(1, 1, At, B1); PG8_BAR; PG8_SCHED;
	s_waitcnt lgkmcnt(0)
	v_mfma_f32_16x16x32_bf16 v[126:129], v[146:149], v[188:191], v[126:129]
	v_mfma_f32_16x16x32_bf16 v[122:125], v[162:165], v[188:191], v[122:125]
	v_mfma_f32_16x16x32_bf16 v[110:113], v[146:149], v[196:199], v[110:113]
	v_mfma_f32_16x16x32_bf16 v[106:109], v[162:165], v[196:199], v[106:109]
	v_mfma_f32_16x16x32_bf16 v[94:97], v[146:149], v[204:207], v[94:97]
	v_mfma_f32_16x16x32_bf16 v[90:93], v[162:165], v[204:207], v[90:93]
	v_mfma_f32_16x16x32_bf16 v[78:81], v[146:149], v[212:215], v[78:81]
	v_mfma_f32_16x16x32_bf16 v[74:77], v[162:165], v[212:215], v[74:77]
	v_mfma_f32_16x16x32_bf16 v[126:129], v[158:161], v[192:195], v[126:129]
	v_mfma_f32_16x16x32_bf16 v[122:125], v[166:169], v[192:195], v[122:125]
	v_mfma_f32_16x16x32_bf16 v[110:113], v[158:161], v[200:203], v[110:113]
	v_mfma_f32_16x16x32_bf16 v[106:109], v[166:169], v[200:203], v[106:109]
	v_mfma_f32_16x16x32_bf16 v[94:97], v[158:161], v[208:211], v[94:97]
	v_mfma_f32_16x16x32_bf16 v[90:93], v[166:169], v[208:211], v[90:93]
	v_mfma_f32_16x16x32_bf16 v[78:81], v[158:161], v[216:219], v[78:81]
	v_mfma_f32_16x16x32_bf16 v[74:77], v[166:169], v[216:219], v[74:77]
	v_mfma_f32_16x16x32_bf16 v[118:121], v[170:173], v[188:191], v[118:121]
	v_mfma_f32_16x16x32_bf16 v[114:117], v[178:181], v[188:191], v[114:117]
	v_mfma_f32_16x16x32_bf16 v[102:105], v[170:173], v[196:199], v[102:105]
	v_mfma_f32_16x16x32_bf16 v[98:101], v[178:181], v[196:199], v[98:101]
	v_mfma_f32_16x16x32_bf16 v[86:89], v[170:173], v[204:207], v[86:89]
	v_mfma_f32_16x16x32_bf16 v[82:85], v[178:181], v[204:207], v[82:85]
	v_mfma_f32_16x16x32_bf16 v[70:73], v[170:173], v[212:215], v[70:73]
	v_mfma_f32_16x16x32_bf16 v[66:69], v[178:181], v[212:215], v[66:69]
	v_mfma_f32_16x16x32_bf16 v[118:121], v[174:177], v[192:195], v[118:121]
	v_mfma_f32_16x16x32_bf16 v[114:117], v[184:187], v[192:195], v[114:117]
	v_mfma_f32_16x16x32_bf16 v[102:105], v[174:177], v[200:203], v[102:105]
	v_mfma_f32_16x16x32_bf16 v[98:101], v[184:187], v[200:203], v[98:101]
	v_mfma_f32_16x16x32_bf16 v[86:89], v[174:177], v[208:211], v[86:89]
	v_mfma_f32_16x16x32_bf16 v[82:85], v[184:187], v[208:211], v[82:85]
	v_mfma_f32_16x16x32_bf16 v[70:73], v[174:177], v[216:219], v[70:73]
	v_mfma_f32_16x16x32_bf16 v[66:69], v[184:187], v[216:219], v[66:69]
	s_barrier
	s_add_i32 s52, s44, s36
	s_nop 0
	s_mov_b32 m0, s52
	ds_read_b128 v[188:191], v156 offset:16384
	ds_read_b128 v[192:195], v156 offset:17408
	ds_read_b128 v[196:199], v156 offset:18432
	ds_read_b128 v[200:203], v156 offset:19456
	ds_read_b128 v[204:207], v156 offset:20480
	ds_read_b128 v[208:211], v156 offset:21504
	ds_read_b128 v[212:215], v156 offset:22528
	ds_read_b128 v[216:219], v156 offset:23552
	global_load_lds_dwordx4 v132, s[30:31]
	s_add_i32 m0, s52, 0x2000
	s_add_u32 s52, s30, 0x200000
	s_nop 0
	s_addc_u32 s53, s31, 0
	s_add_i32 s54, s45, s36
	global_load_lds_dwordx4 v136, s[30:31]
	s_nop 0
	s_mov_b32 m0, s54
	s_add_u32 s60, s34, s2
	s_addc_u32 s61, s35, s3
	global_load_lds_dwordx4 v132, s[52:53]
	s_nop 0
	s_add_i32 m0, s54, 0x2000
	s_nop 0
	global_load_lds_dwordx4 v136, s[52:53]
	s_nop 0
	s_mov_b32 m0, s27
	s_nop 0
	global_load_lds_dwordx4 v130, s[34:35]
	s_mov_b32 m0, s37
	s_nop 0
	global_load_lds_dwordx4 v134, s[34:35]
	s_waitcnt vmcnt(8)
	s_waitcnt lgkmcnt(0)
	s_barrier
	s_waitcnt lgkmcnt(0)
	v_mfma_f32_16x16x32_bf16 v[62:65], v[146:149], v[188:191], v[62:65]
	v_mfma_f32_16x16x32_bf16 v[58:61], v[162:165], v[188:191], v[58:61]
	v_mfma_f32_16x16x32_bf16 v[46:49], v[146:149], v[196:199], v[46:49]
	v_mfma_f32_16x16x32_bf16 v[42:45], v[162:165], v[196:199], v[42:45]
	v_mfma_f32_16x16x32_bf16 v[30:33], v[146:149], v[204:207], v[30:33]
	v_mfma_f32_16x16x32_bf16 v[26:29], v[162:165], v[204:207], v[26:29]
	v_mfma_f32_16x16x32_bf16 v[14:17], v[146:149], v[212:215], v[14:17]
	v_mfma_f32_16x16x32_bf16 v[10:13], v[162:165], v[212:215], v[10:13]
	v_mfma_f32_16x16x32_bf16 v[62:65], v[158:161], v[192:195], v[62:65]
	v_mfma_f32_16x16x32_bf16 v[58:61], v[166:169], v[192:195], v[58:61]
	v_mfma_f32_16x16x32_bf16 v[46:49], v[158:161], v[200:203], v[46:49]
	v_mfma_f32_16x16x32_bf16 v[42:45], v[166:169], v[200:203], v[42:45]
	v_mfma_f32_16x16x32_bf16 v[30:33], v[158:161], v[208:211], v[30:33]
	v_mfma_f32_16x16x32_bf16 v[26:29], v[166:169], v[208:211], v[26:29]
	v_mfma_f32_16x16x32_bf16 v[14:17], v[158:161], v[216:219], v[14:17]
	v_mfma_f32_16x16x32_bf16 v[10:13], v[166:169], v[216:219], v[10:13]
	v_mfma_f32_16x16x32_bf16 v[54:57], v[170:173], v[188:191], v[54:57]
	v_mfma_f32_16x16x32_bf16 v[50:53], v[178:181], v[188:191], v[50:53]
	v_mfma_f32_16x16x32_bf16 v[38:41], v[170:173], v[196:199], v[38:41]
	v_mfma_f32_16x16x32_bf16 v[34:37], v[178:181], v[196:199], v[34:37]
	v_mfma_f32_16x16x32_bf16 v[22:25], v[170:173], v[204:207], v[22:25]
	v_mfma_f32_16x16x32_bf16 v[18:21], v[178:181], v[204:207], v[18:21]
	v_mfma_f32_16x16x32_bf16 v[6:9], v[170:173], v[212:215], v[6:9]
	v_mfma_f32_16x16x32_bf16 v[2:5], v[178:181], v[212:215], v[2:5]
	v_mfma_f32_16x16x32_bf16 v[54:57], v[174:177], v[192:195], v[54:57]
	v_mfma_f32_16x16x32_bf16 v[50:53], v[184:187], v[192:195], v[50:53]
	v_mfma_f32_16x16x32_bf16 v[38:41], v[174:177], v[200:203], v[38:41]
	v_mfma_f32_16x16x32_bf16 v[34:37], v[184:187], v[200:203], v[34:37]
	v_mfma_f32_16x16x32_bf16 v[22:25], v[174:177], v[208:211], v[22:25]
	v_mfma_f32_16x16x32_bf16 v[18:21], v[184:187], v[208:211], v[18:21]
	v_mfma_f32_16x16x32_bf16 v[6:9], v[174:177], v[216:219], v[6:9]
	v_mfma_f32_16x16x32_bf16 v[2:5], v[184:187], v[216:219], v[2:5]
	s_barrier
; #define PG8_STAGE(bufoff, gbase, voff) do { _Pragma("unroll") for (int _i = 0; _i < 2; ++_i) \
;         __builtin_amdgcn_global_load_lds((const unsigned*)((const char*)(gbase) + (voff)[_i]), (PG8_LAS unsigned*)(lds + (bufoff) + ldsw + _i * 8192), 16, 0, 0); } while (0)
; #define PG8_LDA(dst, b, h) do { _Pragma("unroll") for (int m = 0; m < 4; ++m) _Pragma("unroll") for (int k = 0; k < 2; ++k) dst[m][k] = *(const PG8_LAS bf16x8*)(lds + PG8_SA(b, h) + aoff + m * 2048 + k * 1024); } while (0)
; #define PG8_LDB(dst, b, h) do { _Pragma("unroll") for (int n = 0; n < 2; ++n) _Pragma("unroll") for (int k = 0; k < 2; ++k) dst[n][k] = *(const PG8_LAS bf16x8*)(lds + PG8_SB(b, h) + boff + n * 2048 + k * 1024); } while (0)
; #define PG8_MMA(ai, bj, At, Bt) do { __builtin_amdgcn_s_setprio(1); _Pragma("unroll") for (int m = 0; m < 4; ++m) _Pragma("unroll") for (int n = 0; n < 2; ++n) _Pragma("unroll") for (int k = 0; k < 2; ++k) \
;         acc[ai][bj][m][n] = __builtin_amdgcn_mfma_f32_16x16x32_bf16(Bt[n][k], At[m][k], acc[ai][bj][m][n], 0, 0, 0); __builtin_amdgcn_s_setprio(0); } while (0)
; #define PG8_WAIT_V(n) asm volatile("s_waitcnt vmcnt(" #n ")" ::: "memory")
; #define PG8_WAIT_L(n) asm volatile("s_waitcnt lgkmcnt(" #n ")" ::: "memory")
; #define PG8_BAR __builtin_amdgcn_s_barrier()
; #define PG8_SCHED __builtin_amdgcn_sched_barrier(0)
; template <class Epi, class Sched, bool ALIGN_EPI = false, bool SP2 = false>
; __device__ __forceinline__ void gemm_phase(PG8_LAS unsigned char* lds, const Gemm g, const Sched& S, const Epi& E) {
;     ...
;             PG8_LDB(B0, 1, 0); PG8_LDB(B1, 1, 1); PG8_SCHED; PG8_LDA(At, 1, 0); PG8_STAGE(PG8_SA(0, 1), a2 + hstep, voffA);
;             PG8_WAIT_V(8); PG8_WAIT_L(0); PG8_BAR; PG8_MMA(0, 0, At, B0); PG8_MMA(0, 1, At, B1); PG8_BAR; PG8_SCHED;
;             PG8_LDA(At, 1, 1); PG8_STAGE(PG8_SB(1, 0), b3, voffB); PG8_STAGE(PG8_SB(1, 1), b3 + hstep, voffB); PG8_STAGE(PG8_SA(1, 0), a3, voffA);
;             PG8_WAIT_V(8); PG8_WAIT_L(0); PG8_BAR; PG8_MMA(1, 0, At, B0); PG8_MMA(1, 1, At, B1); PG8_BAR; PG8_SCHED;
	s_add_i32 s52, 0, 0x18000
	v_add_u32_e32 v157, s52, v152
	s_add_i32 s53, 0, 0x1c000
	ds_read_b128 v[146:149], v157
	ds_read_b128 v[158:161], v157 offset:1024
	ds_read_b128 v[162:165], v157 offset:2048
	ds_read_b128 v[166:169], v157 offset:3072
	v_add_u32_e32 v157, s53, v152
	ds_read_b128 v[170:173], v157
	ds_read_b128 v[174:177], v157 offset:1024
	ds_read_b128 v[178:181], v157 offset:2048
	ds_read_b128 v[184:187], v157 offset:3072
	s_add_u32 s34, s34, 0x200000
	s_addc_u32 s35, s35, 0
	s_mov_b32 m0, s38
	s_nop 0
	ds_read_b128 v[188:191], v156 offset:32768
	ds_read_b128 v[192:195], v156 offset:33792
	ds_read_b128 v[196:199], v156 offset:34816
	ds_read_b128 v[200:203], v156 offset:35840
	ds_read_b128 v[204:207], v156 offset:36864
	ds_read_b128 v[208:211], v156 offset:37888
	ds_read_b128 v[212:215], v156 offset:38912
	ds_read_b128 v[216:219], v156 offset:39936
	global_load_lds_dwordx4 v130, s[34:35]
	s_nop 0
	s_mov_b32 m0, s39
	s_nop 0
	global_load_lds_dwordx4 v134, s[34:35]
	s_waitcnt vmcnt(8)
	s_waitcnt lgkmcnt(0)
	s_barrier
	s_waitcnt lgkmcnt(0)
	v_mfma_f32_16x16x32_bf16 v[126:129], v[146:149], v[188:191], v[126:129]
	v_mfma_f32_16x16x32_bf16 v[122:125], v[162:165], v[188:191], v[122:125]
	v_mfma_f32_16x16x32_bf16 v[110:113], v[146:149], v[196:199], v[110:113]
	v_mfma_f32_16x16x32_bf16 v[106:109], v[162:165], v[196:199], v[106:109]
	v_mfma_f32_16x16x32_bf16 v[94:97], v[146:149], v[204:207], v[94:97]
	v_mfma_f32_16x16x32_bf16 v[90:93], v[162:165], v[204:207], v[90:93]
	v_mfma_f32_16x16x32_bf16 v[78:81], v[146:149], v[212:215], v[78:81]
	v_mfma_f32_16x16x32_bf16 v[74:77], v[162:165], v[212:215], v[74:77]
	v_mfma_f32_16x16x32_bf16 v[126:129], v[158:161], v[192:195], v[126:129]
	v_mfma_f32_16x16x32_bf16 v[122:125], v[166:169], v[192:195], v[122:125]
	v_mfma_f32_16x16x32_bf16 v[110:113], v[158:161], v[200:203], v[110:113]
	v_mfma_f32_16x16x32_bf16 v[106:109], v[166:169], v[200:203], v[106:109]
	v_mfma_f32_16x16x32_bf16 v[94:97], v[158:161], v[208:211], v[94:97]
	v_mfma_f32_16x16x32_bf16 v[90:93], v[166:169], v[208:211], v[90:93]
	v_mfma_f32_16x16x32_bf16 v[78:81], v[158:161], v[216:219], v[78:81]
	v_mfma_f32_16x16x32_bf16 v[74:77], v[166:169], v[216:219], v[74:77]
	v_mfma_f32_16x16x32_bf16 v[118:121], v[170:173], v[188:191], v[118:121]
	v_mfma_f32_16x16x32_bf16 v[114:117], v[178:181], v[188:191], v[114:117]
	v_mfma_f32_16x16x32_bf16 v[102:105], v[170:173], v[196:199], v[102:105]
	v_mfma_f32_16x16x32_bf16 v[98:101], v[178:181], v[196:199], v[98:101]
	v_mfma_f32_16x16x32_bf16 v[86:89], v[170:173], v[204:207], v[86:89]
	v_mfma_f32_16x16x32_bf16 v[82:85], v[178:181], v[204:207], v[82:85]
	v_mfma_f32_16x16x32_bf16 v[70:73], v[170:173], v[212:215], v[70:73]
	v_mfma_f32_16x16x32_bf16 v[66:69], v[178:181], v[212:215], v[66:69]
	v_mfma_f32_16x16x32_bf16 v[118:121], v[174:177], v[192:195], v[118:121]
	v_mfma_f32_16x16x32_bf16 v[114:117], v[184:187], v[192:195], v[114:117]
	v_mfma_f32_16x16x32_bf16 v[102:105], v[174:177], v[200:203], v[102:105]
	v_mfma_f32_16x16x32_bf16 v[98:101], v[184:187], v[200:203], v[98:101]
	v_mfma_f32_16x16x32_bf16 v[86:89], v[174:177], v[208:211], v[86:89]
	v_mfma_f32_16x16x32_bf16 v[82:85], v[184:187], v[208:211], v[82:85]
	v_mfma_f32_16x16x32_bf16 v[70:73], v[174:177], v[216:219], v[70:73]
	v_mfma_f32_16x16x32_bf16 v[66:69], v[184:187], v[216:219], v[66:69]
	s_barrier
	s_add_i32 s34, s52, s36
	s_add_u32 s58, s30, s2
	s_addc_u32 s59, s31, s3
	s_mov_b32 m0, s34
	ds_read_b128 v[188:191], v156 offset:49152
	ds_read_b128 v[192:195], v156 offset:50176
	ds_read_b128 v[196:199], v156 offset:51200
	ds_read_b128 v[200:203], v156 offset:52224
	ds_read_b128 v[204:207], v156 offset:53248
	ds_read_b128 v[208:211], v156 offset:54272
	ds_read_b128 v[212:215], v156 offset:55296
	ds_read_b128 v[216:219], v156 offset:56320
	global_load_lds_dwordx4 v132, s[58:59]
	s_add_i32 m0, s34, 0x2000
	s_add_u32 s30, s30, 0x200080
	s_nop 0
	s_addc_u32 s31, s31, 0
	s_add_i32 s34, s53, s36
	global_load_lds_dwordx4 v136, s[58:59]
	s_nop 0
	s_mov_b32 m0, s34
	s_nop 0
	global_load_lds_dwordx4 v132, s[30:31]
	s_nop 0
	s_add_i32 m0, s34, 0x2000
	s_nop 0
	global_load_lds_dwordx4 v136, s[30:31]
	s_nop 0
	s_mov_b32 m0, s41
	s_nop 0
	global_load_lds_dwordx4 v130, s[60:61]
	s_nop 0
	s_mov_b32 m0, s42
	s_nop 0
	global_load_lds_dwordx4 v134, s[60:61]
	s_waitcnt vmcnt(8)
	s_waitcnt lgkmcnt(0)
	s_barrier
	s_waitcnt lgkmcnt(0)
	v_mfma_f32_16x16x32_bf16 v[62:65], v[146:149], v[188:191], v[62:65]
	v_mfma_f32_16x16x32_bf16 v[58:61], v[162:165], v[188:191], v[58:61]
	v_mfma_f32_16x16x32_bf16 v[46:49], v[146:149], v[196:199], v[46:49]
	v_mfma_f32_16x16x32_bf16 v[42:45], v[162:165], v[196:199], v[42:45]
	v_mfma_f32_16x16x32_bf16 v[30:33], v[146:149], v[204:207], v[30:33]
	v_mfma_f32_16x16x32_bf16 v[26:29], v[162:165], v[204:207], v[26:29]
	v_mfma_f32_16x16x32_bf16 v[14:17], v[146:149], v[212:215], v[14:17]
	v_mfma_f32_16x16x32_bf16 v[10:13], v[162:165], v[212:215], v[10:13]
	v_mfma_f32_16x16x32_bf16 v[62:65], v[158:161], v[192:195], v[62:65]
	v_mfma_f32_16x16x32_bf16 v[58:61], v[166:169], v[192:195], v[58:61]
	v_mfma_f32_16x16x32_bf16 v[46:49], v[158:161], v[200:203], v[46:49]
	v_mfma_f32_16x16x32_bf16 v[42:45], v[166:169], v[200:203], v[42:45]
	v_mfma_f32_16x16x32_bf16 v[30:33], v[158:161], v[208:211], v[30:33]
	v_mfma_f32_16x16x32_bf16 v[26:29], v[166:169], v[208:211], v[26:29]
	v_mfma_f32_16x16x32_bf16 v[14:17], v[158:161], v[216:219], v[14:17]
	v_mfma_f32_16x16x32_bf16 v[10:13], v[166:169], v[216:219], v[10:13]
	v_mfma_f32_16x16x32_bf16 v[54:57], v[170:173], v[188:191], v[54:57]
	v_mfma_f32_16x16x32_bf16 v[50:53], v[178:181], v[188:191], v[50:53]
	v_mfma_f32_16x16x32_bf16 v[38:41], v[170:173], v[196:199], v[38:41]
	v_mfma_f32_16x16x32_bf16 v[34:37], v[178:181], v[196:199], v[34:37]
	v_mfma_f32_16x16x32_bf16 v[22:25], v[170:173], v[204:207], v[22:25]
	v_mfma_f32_16x16x32_bf16 v[18:21], v[178:181], v[204:207], v[18:21]
	v_mfma_f32_16x16x32_bf16 v[6:9], v[170:173], v[212:215], v[6:9]
	v_mfma_f32_16x16x32_bf16 v[2:5], v[178:181], v[212:215], v[2:5]
	v_mfma_f32_16x16x32_bf16 v[54:57], v[174:177], v[192:195], v[54:57]
	v_mfma_f32_16x16x32_bf16 v[50:53], v[184:187], v[192:195], v[50:53]
	v_mfma_f32_16x16x32_bf16 v[38:41], v[174:177], v[200:203], v[38:41]
	v_mfma_f32_16x16x32_bf16 v[34:37], v[184:187], v[200:203], v[34:37]
	v_mfma_f32_16x16x32_bf16 v[22:25], v[174:177], v[208:211], v[22:25]
	v_mfma_f32_16x16x32_bf16 v[18:21], v[184:187], v[208:211], v[18:21]
	v_mfma_f32_16x16x32_bf16 v[6:9], v[174:177], v[216:219], v[6:9]
	v_mfma_f32_16x16x32_bf16 v[2:5], v[184:187], v[216:219], v[2:5]
	s_barrier
	s_add_i32 s51, s51, 2
	s_add_u32 s28, s28, 0x100
	s_addc_u32 s29, s29, 0
	s_add_u32 s49, s49, 0x100
	s_addc_u32 s50, s50, 0
	s_cmpk_gt_u32 s51, 0x7d
	s_cbranch_scc0 .LBB0_563
	s_and_b64 vcc, exec, s[8:9]
	s_cbranch_vccz .LBB0_566
	s_barrier

; #define PG8_STAGE(bufoff, gbase, voff) do { _Pragma("unroll") for (int _i = 0; _i < 2; ++_i) \
;         __builtin_amdgcn_global_load_lds((const unsigned*)((const char*)(gbase) + (voff)[_i]), (PG8_LAS unsigned*)(lds + (bufoff) + ldsw + _i * 8192), 16, 0, 0); } while (0)
; #define PG8_LDA(dst, b, h) do { _Pragma("unroll") for (int m = 0; m < 4; ++m) _Pragma("unroll") for (int k = 0; k < 2; ++k) dst[m][k] = *(const PG8_LAS bf16x8*)(lds + PG8_SA(b, h) + aoff + m * 2048 + k * 1024); } while (0)
; #define PG8_LDB(dst, b, h) do { _Pragma("unroll") for (int n = 0; n < 2; ++n) _Pragma("unroll") for (int k = 0; k < 2; ++k) dst[n][k] = *(const PG8_LAS bf16x8*)(lds + PG8_SB(b, h) + boff + n * 2048 + k * 1024); } while (0)
; #define PG8_WAIT_V(n) asm volatile("s_waitcnt vmcnt(" #n ")" ::: "memory")
; #define PG8_WAIT_L(n) asm volatile("s_waitcnt lgkmcnt(" #n ")" ::: "memory")
; #define PG8_BAR __builtin_amdgcn_s_barrier()
; #define PG8_SCHED __builtin_amdgcn_sched_barrier(0)
; template <class Epi, class Sched, bool ALIGN_EPI = false, bool SP2 = false>
; __device__ __forceinline__ void gemm_phase(PG8_LAS unsigned char* lds, const Gemm g, const Sched& S, const Epi& E) {
;     ...
;         const char* nA = has_next ? (const char*)g.A + (size_t)nxt.pm * tstep : cA; const char* nB = has_next ? (const char*)g.Bt + (size_t)nxt.pn * tstep : cB;
;         for (int t = 0; t < nt; t += 2) {
;             const bool last = (t == nt - 2);
;             const char* a1 = cA + (size_t)(t + 1) * kstep;
;             const char* a2 = last ? nA : cA + (size_t)(t + 2) * kstep; const char* b2 = last ? nB : cB + (size_t)(t + 2) * kstep;
;             const char* a3 = a2 + kstep; const char* b3 = b2 + kstep;
;             if (last && has_next) S.a_ready(nxt);
;             if constexpr (SP2) {
;             PG8_LDB(B0, 0, 0); PG8_LDB(B1, 0, 1); PG8_SCHED; PG8_LDA(At, 0, 0); PG8_STAGE(PG8_SA(1, 1), a1 + hstep, voffA);
;             PG8_WAIT_V(8); PG8_WAIT_L(0); PG8_BAR; PG8_MMA(0, 0, At, B0); PG8_MMA(0, 1, At, B1); PG8_BAR; PG8_SCHED;
;     ...
; #pragma unroll
;         for (int a = 0; a < 2; ++a)
; #pragma unroll
;             for (int b = 0; b < 2; ++b)
; #pragma unroll
;                 for (int m = 0; m < 4; ++m)
; #pragma unroll
;                     for (int n = 0; n < 2; ++n) acc[a][b][m][n] = (f32x4){0.f, 0.f, 0.f, 0.f};
;         cur = nxt; cA = nA; cB = nB; ++ui;
.LBB0_706:
	s_ashr_i32 s25, s24, 31
	s_lshl_b64 s[26:27], s[24:25], 21
	s_add_u32 s26, s6, s26
	s_addc_u32 s27, s7, s27
	s_and_b64 s[28:29], s[4:5], exec
	s_cselect_b32 s25, s27, s31
	s_cselect_b32 s57, s26, s30
	s_ashr_i32 s23, s22, 31
	s_lshl_b64 s[28:29], s[22:23], 21
	v_readlane_b32 s23, v249, 30
	s_add_u32 s28, s23, s28
	v_readlane_b32 s23, v249, 31
	s_addc_u32 s29, s23, s29
	s_and_b64 s[36:37], s[4:5], exec
	s_cselect_b32 s23, s29, s35
	s_cselect_b32 s58, s28, s34
	s_add_u32 s30, s30, 0x100080
	s_addc_u32 s31, s31, 0
	s_add_u32 s59, s34, 0x100
	v_mov_b32_e32 v2, 0
	s_addc_u32 s60, s35, 0
	s_mov_b32 s61, -2
	v_mov_b32_e32 v3, v2
	v_mov_b32_e32 v4, v2
	v_mov_b32_e32 v5, v2
	v_mov_b32_e32 v6, v2
	v_mov_b32_e32 v7, v2
	v_mov_b32_e32 v8, v2
	v_mov_b32_e32 v9, v2
	v_mov_b32_e32 v18, v2
	v_mov_b32_e32 v19, v2
	v_mov_b32_e32 v20, v2
	v_mov_b32_e32 v21, v2
	v_mov_b32_e32 v22, v2
	v_mov_b32_e32 v23, v2
	v_mov_b32_e32 v24, v2
	v_mov_b32_e32 v25, v2
	v_mov_b32_e32 v30, v2
	v_mov_b32_e32 v31, v2
	v_mov_b32_e32 v32, v2
	v_mov_b32_e32 v33, v2
	v_mov_b32_e32 v38, v2
	v_mov_b32_e32 v39, v2
	v_mov_b32_e32 v40, v2
	v_mov_b32_e32 v41, v2
	v_mov_b32_e32 v46, v2
	v_mov_b32_e32 v47, v2
	v_mov_b32_e32 v48, v2
	v_mov_b32_e32 v49, v2
	v_mov_b32_e32 v54, v2
	v_mov_b32_e32 v55, v2
	v_mov_b32_e32 v56, v2
	v_mov_b32_e32 v57, v2
	v_mov_b32_e32 v10, v2
	v_mov_b32_e32 v11, v2
	v_mov_b32_e32 v12, v2
	v_mov_b32_e32 v13, v2
	v_mov_b32_e32 v14, v2
	v_mov_b32_e32 v15, v2
	v_mov_b32_e32 v16, v2
	v_mov_b32_e32 v17, v2
	v_mov_b32_e32 v26, v2
	v_mov_b32_e32 v27, v2
	v_mov_b32_e32 v28, v2
	v_mov_b32_e32 v29, v2
	v_mov_b32_e32 v34, v2
	v_mov_b32_e32 v35, v2
	v_mov_b32_e32 v36, v2
	v_mov_b32_e32 v37, v2
	v_mov_b32_e32 v42, v2
	v_mov_b32_e32 v43, v2
	v_mov_b32_e32 v44, v2
	v_mov_b32_e32 v45, v2
	v_mov_b32_e32 v50, v2
	v_mov_b32_e32 v51, v2
	v_mov_b32_e32 v52, v2
	v_mov_b32_e32 v53, v2
	v_mov_b32_e32 v58, v2
	v_mov_b32_e32 v59, v2
	v_mov_b32_e32 v60, v2
	v_mov_b32_e32 v61, v2
	v_mov_b32_e32 v62, v2
	v_mov_b32_e32 v63, v2
	v_mov_b32_e32 v64, v2
	v_mov_b32_e32 v65, v2
	s_waitcnt vmcnt(0)
	v_mov_b32_e32 v66, v2
	v_mov_b32_e32 v67, v2
	v_mov_b32_e32 v68, v2
	v_mov_b32_e32 v69, v2
	v_mov_b32_e32 v70, v2
	v_mov_b32_e32 v71, v2
	v_mov_b32_e32 v72, v2
	v_mov_b32_e32 v73, v2
	v_mov_b32_e32 v74, v2
	v_mov_b32_e32 v75, v2
	v_mov_b32_e32 v76, v2
	v_mov_b32_e32 v77, v2
	v_mov_b32_e32 v82, v2
	v_mov_b32_e32 v83, v2
	v_mov_b32_e32 v84, v2
	v_mov_b32_e32 v85, v2
	v_mov_b32_e32 v98, v2
	v_mov_b32_e32 v99, v2
	v_mov_b32_e32 v100, v2
	v_mov_b32_e32 v101, v2
	v_mov_b32_e32 v102, v2
	v_mov_b32_e32 v103, v2
	v_mov_b32_e32 v104, v2
	v_mov_b32_e32 v105, v2
	v_mov_b32_e32 v114, v2
	v_mov_b32_e32 v115, v2
	v_mov_b32_e32 v116, v2
	v_mov_b32_e32 v117, v2
	v_mov_b32_e32 v118, v2
	v_mov_b32_e32 v119, v2
	v_mov_b32_e32 v120, v2
	v_mov_b32_e32 v121, v2
	v_mov_b32_e32 v78, v2
	v_mov_b32_e32 v79, v2
	v_mov_b32_e32 v80, v2
	v_mov_b32_e32 v81, v2
	v_mov_b32_e32 v86, v2
	v_mov_b32_e32 v87, v2
	v_mov_b32_e32 v88, v2
	v_mov_b32_e32 v89, v2
	v_mov_b32_e32 v90, v2
	v_mov_b32_e32 v91, v2
	v_mov_b32_e32 v92, v2
	v_mov_b32_e32 v93, v2
	v_mov_b32_e32 v94, v2
	v_mov_b32_e32 v95, v2
	v_mov_b32_e32 v96, v2
	v_mov_b32_e32 v97, v2
	v_mov_b32_e32 v106, v2
	v_mov_b32_e32 v107, v2
	v_mov_b32_e32 v108, v2
	v_mov_b32_e32 v109, v2
	v_mov_b32_e32 v110, v2
	v_mov_b32_e32 v111, v2
	v_mov_b32_e32 v112, v2
	v_mov_b32_e32 v113, v2
	v_mov_b32_e32 v122, v2
	v_mov_b32_e32 v123, v2
	v_mov_b32_e32 v124, v2
	v_mov_b32_e32 v125, v2
	v_mov_b32_e32 v126, v2
	v_mov_b32_e32 v127, v2
	v_mov_b32_e32 v128, v2
	v_mov_b32_e32 v129, v2
	s_nop 0
	s_nop 0
	s_nop 0
	s_nop 0
	s_nop 0
	s_nop 0
	s_nop 0
	s_nop 0
	s_nop 0
	s_nop 0
	s_nop 0
	s_nop 0
	s_nop 0
	s_nop 0
	s_nop 0
	s_nop 0
	s_nop 0
	s_nop 0
	s_nop 0
	s_nop 0
	s_nop 0
	s_nop 0
.LBB0_707:
	ds_read_b128 v[142:145], v151
	ds_read_b128 v[154:157], v151 offset:1024
	ds_read_b128 v[158:161], v151 offset:2048
	ds_read_b128 v[162:165], v151 offset:3072
	ds_read_b128 v[166:169], v152
	ds_read_b128 v[170:173], v152 offset:1024
	ds_read_b128 v[174:177], v152 offset:2048
	ds_read_b128 v[178:181], v152 offset:3072
	s_add_u32 s34, s30, 0xfff00080
	s_addc_u32 s35, s31, -1
	s_cmp_eq_u32 s61, 60
	s_cselect_b32 s37, s25, s35
	s_cselect_b32 s36, s57, s34
	s_cselect_b32 s35, s23, s60
	s_cselect_b32 s34, s58, s59
	s_nop 0
	s_add_i32 m0, s42, 0xc000
	ds_read_b128 v[184:187], v153
	ds_read_b128 v[188:191], v153 offset:1024
	ds_read_b128 v[192:195], v153 offset:2048
	ds_read_b128 v[196:199], v153 offset:3072
	ds_read_b128 v[200:203], v153 offset:4096
	ds_read_b128 v[204:207], v153 offset:5120
	ds_read_b128 v[208:211], v153 offset:6144
	ds_read_b128 v[212:215], v153 offset:7168
	global_load_lds_dwordx4 v134, s[30:31]
	s_nop 0
	s_add_i32 m0, s42, 0xe000
	s_nop 0
	global_load_lds_dwordx4 v136, s[30:31]
	s_waitcnt vmcnt(8)
	s_waitcnt lgkmcnt(0)
	s_barrier
; #define PG8_STAGE(bufoff, gbase, voff) do { _Pragma("unroll") for (int _i = 0; _i < 2; ++_i) \
;         __builtin_amdgcn_global_load_lds((const unsigned*)((const char*)(gbase) + (voff)[_i]), (PG8_LAS unsigned*)(lds + (bufoff) + ldsw + _i * 8192), 16, 0, 0); } while (0)
; #define PG8_LDA(dst, b, h) do { _Pragma("unroll") for (int m = 0; m < 4; ++m) _Pragma("unroll") for (int k = 0; k < 2; ++k) dst[m][k] = *(const PG8_LAS bf16x8*)(lds + PG8_SA(b, h) + aoff + m * 2048 + k * 1024); } while (0)
; #define PG8_MMA(ai, bj, At, Bt) do { __builtin_amdgcn_s_setprio(1); _Pragma("unroll") for (int m = 0; m < 4; ++m) _Pragma("unroll") for (int n = 0; n < 2; ++n) _Pragma("unroll") for (int k = 0; k < 2; ++k) \
;         acc[ai][bj][m][n] = __builtin_amdgcn_mfma_f32_16x16x32_bf16(Bt[n][k], At[m][k], acc[ai][bj][m][n], 0, 0, 0); __builtin_amdgcn_s_setprio(0); } while (0)
; #define PG8_WAIT_V(n) asm volatile("s_waitcnt vmcnt(" #n ")" ::: "memory")
; #define PG8_WAIT_L(n) asm volatile("s_waitcnt lgkmcnt(" #n ")" ::: "memory")
; #define PG8_BAR __builtin_amdgcn_s_barrier()
; #define PG8_SCHED __builtin_amdgcn_sched_barrier(0)
; template <class Epi, class Sched, bool ALIGN_EPI = false, bool SP2 = false>
; __device__ __forceinline__ void gemm_phase(PG8_LAS unsigned char* lds, const Gemm g, const Sched& S, const Epi& E) {
;     ...
;             PG8_WAIT_V(8); PG8_WAIT_L(0); PG8_BAR; PG8_MMA(0, 0, At, B0); PG8_MMA(0, 1, At, B1); PG8_BAR; PG8_SCHED;
;             PG8_LDA(At, 0, 1); PG8_STAGE(PG8_SB(0, 0), b2, voffB); PG8_STAGE(PG8_SB(0, 1), b2 + hstep, voffB); PG8_STAGE(PG8_SA(0, 0), a2, voffA);
;             PG8_WAIT_V(8); PG8_WAIT_L(0); PG8_BAR; PG8_MMA(1, 0, At, B0); PG8_MMA(1, 1, At, B1); PG8_BAR; PG8_SCHED;
	s_waitcnt lgkmcnt(0)
	v_mfma_f32_16x16x32_bf16 v[126:129], v[142:145], v[184:187], v[126:129]
	v_mfma_f32_16x16x32_bf16 v[122:125], v[158:161], v[184:187], v[122:125]
	v_mfma_f32_16x16x32_bf16 v[110:113], v[142:145], v[192:195], v[110:113]
	v_mfma_f32_16x16x32_bf16 v[106:109], v[158:161], v[192:195], v[106:109]
	v_mfma_f32_16x16x32_bf16 v[94:97], v[142:145], v[200:203], v[94:97]
	v_mfma_f32_16x16x32_bf16 v[90:93], v[158:161], v[200:203], v[90:93]
	v_mfma_f32_16x16x32_bf16 v[86:89], v[142:145], v[208:211], v[86:89]
	v_mfma_f32_16x16x32_bf16 v[78:81], v[158:161], v[208:211], v[78:81]
	v_mfma_f32_16x16x32_bf16 v[126:129], v[154:157], v[188:191], v[126:129]
	v_mfma_f32_16x16x32_bf16 v[122:125], v[162:165], v[188:191], v[122:125]
	v_mfma_f32_16x16x32_bf16 v[110:113], v[154:157], v[196:199], v[110:113]
	v_mfma_f32_16x16x32_bf16 v[106:109], v[162:165], v[196:199], v[106:109]
	v_mfma_f32_16x16x32_bf16 v[94:97], v[154:157], v[204:207], v[94:97]
	v_mfma_f32_16x16x32_bf16 v[90:93], v[162:165], v[204:207], v[90:93]
	v_mfma_f32_16x16x32_bf16 v[86:89], v[154:157], v[212:215], v[86:89]
	v_mfma_f32_16x16x32_bf16 v[78:81], v[162:165], v[212:215], v[78:81]
	v_mfma_f32_16x16x32_bf16 v[118:121], v[166:169], v[184:187], v[118:121]
	v_mfma_f32_16x16x32_bf16 v[114:117], v[174:177], v[184:187], v[114:117]
	v_mfma_f32_16x16x32_bf16 v[102:105], v[166:169], v[192:195], v[102:105]
	v_mfma_f32_16x16x32_bf16 v[98:101], v[174:177], v[192:195], v[98:101]
	v_mfma_f32_16x16x32_bf16 v[82:85], v[166:169], v[200:203], v[82:85]
	v_mfma_f32_16x16x32_bf16 v[74:77], v[174:177], v[200:203], v[74:77]
	v_mfma_f32_16x16x32_bf16 v[70:73], v[166:169], v[208:211], v[70:73]
	v_mfma_f32_16x16x32_bf16 v[66:69], v[174:177], v[208:211], v[66:69]
	v_mfma_f32_16x16x32_bf16 v[118:121], v[170:173], v[188:191], v[118:121]
	v_mfma_f32_16x16x32_bf16 v[114:117], v[178:181], v[188:191], v[114:117]
	v_mfma_f32_16x16x32_bf16 v[102:105], v[170:173], v[196:199], v[102:105]
	v_mfma_f32_16x16x32_bf16 v[98:101], v[178:181], v[196:199], v[98:101]
	v_mfma_f32_16x16x32_bf16 v[82:85], v[170:173], v[204:207], v[82:85]
	v_mfma_f32_16x16x32_bf16 v[74:77], v[178:181], v[204:207], v[74:77]
	v_mfma_f32_16x16x32_bf16 v[70:73], v[170:173], v[212:215], v[70:73]
	v_mfma_f32_16x16x32_bf16 v[66:69], v[178:181], v[212:215], v[66:69]
	s_barrier
	s_add_i32 s62, s51, s33
	s_nop 0
	s_mov_b32 m0, s62
	ds_read_b128 v[184:187], v153 offset:16384
	ds_read_b128 v[188:191], v153 offset:17408
	ds_read_b128 v[192:195], v153 offset:18432
	ds_read_b128 v[196:199], v153 offset:19456
	ds_read_b128 v[200:203], v153 offset:20480
	ds_read_b128 v[204:207], v153 offset:21504
	ds_read_b128 v[208:211], v153 offset:22528
	ds_read_b128 v[212:215], v153 offset:23552
	global_load_lds_dwordx4 v130, s[34:35]
	s_add_i32 m0, s62, 0x2000
	s_add_u32 s62, s34, 0x100000
	s_nop 0
	s_addc_u32 s63, s35, 0
	s_add_i32 s72, s52, s33
	global_load_lds_dwordx4 v132, s[34:35]
	s_nop 0
	s_mov_b32 m0, s72
	s_add_u32 s84, s36, s12
	s_addc_u32 s85, s37, s13
	global_load_lds_dwordx4 v130, s[62:63]
	s_nop 0
	s_add_i32 m0, s72, 0x2000
	s_nop 0
	global_load_lds_dwordx4 v132, s[62:63]
	s_nop 0
	s_mov_b32 m0, s42
	s_nop 0
	global_load_lds_dwordx4 v130, s[36:37]
	s_mov_b32 m0, s43
	s_nop 0
	global_load_lds_dwordx4 v132, s[36:37]
	s_waitcnt vmcnt(8)
	s_waitcnt lgkmcnt(0)
	s_barrier
	s_waitcnt lgkmcnt(0)
	v_mfma_f32_16x16x32_bf16 v[62:65], v[142:145], v[184:187], v[62:65]
	v_mfma_f32_16x16x32_bf16 v[58:61], v[158:161], v[184:187], v[58:61]
	v_mfma_f32_16x16x32_bf16 v[50:53], v[142:145], v[192:195], v[50:53]
	v_mfma_f32_16x16x32_bf16 v[42:45], v[158:161], v[192:195], v[42:45]
	v_mfma_f32_16x16x32_bf16 v[34:37], v[142:145], v[200:203], v[34:37]
	v_mfma_f32_16x16x32_bf16 v[26:29], v[158:161], v[200:203], v[26:29]
	v_mfma_f32_16x16x32_bf16 v[14:17], v[142:145], v[208:211], v[14:17]
	v_mfma_f32_16x16x32_bf16 v[10:13], v[158:161], v[208:211], v[10:13]
	v_mfma_f32_16x16x32_bf16 v[62:65], v[154:157], v[188:191], v[62:65]
	v_mfma_f32_16x16x32_bf16 v[58:61], v[162:165], v[188:191], v[58:61]
	v_mfma_f32_16x16x32_bf16 v[50:53], v[154:157], v[196:199], v[50:53]
	v_mfma_f32_16x16x32_bf16 v[42:45], v[162:165], v[196:199], v[42:45]
	v_mfma_f32_16x16x32_bf16 v[34:37], v[154:157], v[204:207], v[34:37]
	v_mfma_f32_16x16x32_bf16 v[26:29], v[162:165], v[204:207], v[26:29]
	v_mfma_f32_16x16x32_bf16 v[14:17], v[154:157], v[212:215], v[14:17]
	v_mfma_f32_16x16x32_bf16 v[10:13], v[162:165], v[212:215], v[10:13]
	v_mfma_f32_16x16x32_bf16 v[54:57], v[166:169], v[184:187], v[54:57]
	v_mfma_f32_16x16x32_bf16 v[46:49], v[174:177], v[184:187], v[46:49]
	v_mfma_f32_16x16x32_bf16 v[38:41], v[166:169], v[192:195], v[38:41]
	v_mfma_f32_16x16x32_bf16 v[30:33], v[174:177], v[192:195], v[30:33]
	v_mfma_f32_16x16x32_bf16 v[22:25], v[166:169], v[200:203], v[22:25]
	v_mfma_f32_16x16x32_bf16 v[18:21], v[174:177], v[200:203], v[18:21]
	v_mfma_f32_16x16x32_bf16 v[6:9], v[166:169], v[208:211], v[6:9]
	v_mfma_f32_16x16x32_bf16 v[2:5], v[174:177], v[208:211], v[2:5]
	v_mfma_f32_16x16x32_bf16 v[54:57], v[170:173], v[188:191], v[54:57]
	v_mfma_f32_16x16x32_bf16 v[46:49], v[178:181], v[188:191], v[46:49]
	v_mfma_f32_16x16x32_bf16 v[38:41], v[170:173], v[196:199], v[38:41]
	v_mfma_f32_16x16x32_bf16 v[30:33], v[178:181], v[196:199], v[30:33]
	v_mfma_f32_16x16x32_bf16 v[22:25], v[170:173], v[204:207], v[22:25]
	v_mfma_f32_16x16x32_bf16 v[18:21], v[178:181], v[204:207], v[18:21]
	v_mfma_f32_16x16x32_bf16 v[6:9], v[170:173], v[212:215], v[6:9]
	v_mfma_f32_16x16x32_bf16 v[2:5], v[178:181], v[212:215], v[2:5]
	s_barrier
; #define PG8_STAGE(bufoff, gbase, voff) do { _Pragma("unroll") for (int _i = 0; _i < 2; ++_i) \
;         __builtin_amdgcn_global_load_lds((const unsigned*)((const char*)(gbase) + (voff)[_i]), (PG8_LAS unsigned*)(lds + (bufoff) + ldsw + _i * 8192), 16, 0, 0); } while (0)
; #define PG8_LDA(dst, b, h) do { _Pragma("unroll") for (int m = 0; m < 4; ++m) _Pragma("unroll") for (int k = 0; k < 2; ++k) dst[m][k] = *(const PG8_LAS bf16x8*)(lds + PG8_SA(b, h) + aoff + m * 2048 + k * 1024); } while (0)
; #define PG8_LDB(dst, b, h) do { _Pragma("unroll") for (int n = 0; n < 2; ++n) _Pragma("unroll") for (int k = 0; k < 2; ++k) dst[n][k] = *(const PG8_LAS bf16x8*)(lds + PG8_SB(b, h) + boff + n * 2048 + k * 1024); } while (0)
; #define PG8_MMA(ai, bj, At, Bt) do { __builtin_amdgcn_s_setprio(1); _Pragma("unroll") for (int m = 0; m < 4; ++m) _Pragma("unroll") for (int n = 0; n < 2; ++n) _Pragma("unroll") for (int k = 0; k < 2; ++k) \
;         acc[ai][bj][m][n] = __builtin_amdgcn_mfma_f32_16x16x32_bf16(Bt[n][k], At[m][k], acc[ai][bj][m][n], 0, 0, 0); __builtin_amdgcn_s_setprio(0); } while (0)
; #define PG8_WAIT_V(n) asm volatile("s_waitcnt vmcnt(" #n ")" ::: "memory")
; #define PG8_WAIT_L(n) asm volatile("s_waitcnt lgkmcnt(" #n ")" ::: "memory")
; #define PG8_BAR __builtin_amdgcn_s_barrier()
; #define PG8_SCHED __builtin_amdgcn_sched_barrier(0)
; template <class Epi, class Sched, bool ALIGN_EPI = false, bool SP2 = false>
; __device__ __forceinline__ void gemm_phase(PG8_LAS unsigned char* lds, const Gemm g, const Sched& S, const Epi& E) {
;     ...
;             PG8_LDB(B0, 1, 0); PG8_LDB(B1, 1, 1); PG8_SCHED; PG8_LDA(At, 1, 0); PG8_STAGE(PG8_SA(0, 1), a2 + hstep, voffA);
;             PG8_WAIT_V(8); PG8_WAIT_L(0); PG8_BAR; PG8_MMA(0, 0, At, B0); PG8_MMA(0, 1, At, B1); PG8_BAR; PG8_SCHED;
;             PG8_LDA(At, 1, 1); PG8_STAGE(PG8_SB(1, 0), b3, voffB); PG8_STAGE(PG8_SB(1, 1), b3 + hstep, voffB); PG8_STAGE(PG8_SA(1, 0), a3, voffA);
;             PG8_WAIT_V(8); PG8_WAIT_L(0); PG8_BAR; PG8_MMA(1, 0, At, B0); PG8_MMA(1, 1, At, B1); PG8_BAR; PG8_SCHED;
	s_add_i32 s62, 0, 0x18000
	s_add_i32 s63, 0, 0x1c000
	v_add_u32_e32 v162, s62, v149
	v_add_u32_e32 v178, s63, v149
	ds_read_b128 v[142:145], v162
	ds_read_b128 v[154:157], v162 offset:1024
	ds_read_b128 v[158:161], v162 offset:2048
	ds_read_b128 v[162:165], v162 offset:3072
	ds_read_b128 v[166:169], v178
	ds_read_b128 v[170:173], v178 offset:1024
	ds_read_b128 v[174:177], v178 offset:2048
	ds_read_b128 v[178:181], v178 offset:3072
	s_add_u32 s36, s36, 0x100000
	s_addc_u32 s37, s37, 0
	s_mov_b32 m0, s44
	s_nop 0
	ds_read_b128 v[184:187], v153 offset:32768
	ds_read_b128 v[188:191], v153 offset:33792
	ds_read_b128 v[192:195], v153 offset:34816
	ds_read_b128 v[196:199], v153 offset:35840
	ds_read_b128 v[200:203], v153 offset:36864
	ds_read_b128 v[204:207], v153 offset:37888
	ds_read_b128 v[208:211], v153 offset:38912
	ds_read_b128 v[212:215], v153 offset:39936
	global_load_lds_dwordx4 v130, s[36:37]
	s_nop 0
	s_mov_b32 m0, s45
	s_nop 0
	global_load_lds_dwordx4 v132, s[36:37]
	s_waitcnt vmcnt(8)
	s_waitcnt lgkmcnt(0)
	s_barrier
	s_waitcnt lgkmcnt(0)
	v_mfma_f32_16x16x32_bf16 v[126:129], v[142:145], v[184:187], v[126:129]
	v_mfma_f32_16x16x32_bf16 v[122:125], v[158:161], v[184:187], v[122:125]
	v_mfma_f32_16x16x32_bf16 v[110:113], v[142:145], v[192:195], v[110:113]
	v_mfma_f32_16x16x32_bf16 v[106:109], v[158:161], v[192:195], v[106:109]
	v_mfma_f32_16x16x32_bf16 v[94:97], v[142:145], v[200:203], v[94:97]
	v_mfma_f32_16x16x32_bf16 v[90:93], v[158:161], v[200:203], v[90:93]
	v_mfma_f32_16x16x32_bf16 v[86:89], v[142:145], v[208:211], v[86:89]
	v_mfma_f32_16x16x32_bf16 v[78:81], v[158:161], v[208:211], v[78:81]
	v_mfma_f32_16x16x32_bf16 v[126:129], v[154:157], v[188:191], v[126:129]
	v_mfma_f32_16x16x32_bf16 v[122:125], v[162:165], v[188:191], v[122:125]
	v_mfma_f32_16x16x32_bf16 v[110:113], v[154:157], v[196:199], v[110:113]
	v_mfma_f32_16x16x32_bf16 v[106:109], v[162:165], v[196:199], v[106:109]
	v_mfma_f32_16x16x32_bf16 v[94:97], v[154:157], v[204:207], v[94:97]
	v_mfma_f32_16x16x32_bf16 v[90:93], v[162:165], v[204:207], v[90:93]
	v_mfma_f32_16x16x32_bf16 v[86:89], v[154:157], v[212:215], v[86:89]
	v_mfma_f32_16x16x32_bf16 v[78:81], v[162:165], v[212:215], v[78:81]
	v_mfma_f32_16x16x32_bf16 v[118:121], v[166:169], v[184:187], v[118:121]
	v_mfma_f32_16x16x32_bf16 v[114:117], v[174:177], v[184:187], v[114:117]
	v_mfma_f32_16x16x32_bf16 v[102:105], v[166:169], v[192:195], v[102:105]
	v_mfma_f32_16x16x32_bf16 v[98:101], v[174:177], v[192:195], v[98:101]
	v_mfma_f32_16x16x32_bf16 v[82:85], v[166:169], v[200:203], v[82:85]
	v_mfma_f32_16x16x32_bf16 v[74:77], v[174:177], v[200:203], v[74:77]
	v_mfma_f32_16x16x32_bf16 v[70:73], v[166:169], v[208:211], v[70:73]
	v_mfma_f32_16x16x32_bf16 v[66:69], v[174:177], v[208:211], v[66:69]
	v_mfma_f32_16x16x32_bf16 v[118:121], v[170:173], v[188:191], v[118:121]
	v_mfma_f32_16x16x32_bf16 v[114:117], v[178:181], v[188:191], v[114:117]
	v_mfma_f32_16x16x32_bf16 v[102:105], v[170:173], v[196:199], v[102:105]
	v_mfma_f32_16x16x32_bf16 v[98:101], v[178:181], v[196:199], v[98:101]
	v_mfma_f32_16x16x32_bf16 v[82:85], v[170:173], v[204:207], v[82:85]
	v_mfma_f32_16x16x32_bf16 v[74:77], v[178:181], v[204:207], v[74:77]
	v_mfma_f32_16x16x32_bf16 v[70:73], v[170:173], v[212:215], v[70:73]
	v_mfma_f32_16x16x32_bf16 v[66:69], v[178:181], v[212:215], v[66:69]
	s_barrier
	s_add_i32 s36, s62, s33
	s_add_u32 s82, s34, s12
	s_addc_u32 s83, s35, s13
	s_mov_b32 m0, s36
	ds_read_b128 v[184:187], v153 offset:49152
	ds_read_b128 v[188:191], v153 offset:50176
	ds_read_b128 v[192:195], v153 offset:51200
	ds_read_b128 v[196:199], v153 offset:52224
	ds_read_b128 v[200:203], v153 offset:53248
	ds_read_b128 v[204:207], v153 offset:54272
	ds_read_b128 v[208:211], v153 offset:55296
	ds_read_b128 v[212:215], v153 offset:56320
	global_load_lds_dwordx4 v130, s[82:83]
	s_add_i32 m0, s36, 0x2000
	s_add_u32 s34, s34, 0x100080
	s_nop 0
	s_addc_u32 s35, s35, 0
	s_add_i32 s36, s63, s33
	global_load_lds_dwordx4 v132, s[82:83]
	s_nop 0
	s_mov_b32 m0, s36
	s_nop 0
	global_load_lds_dwordx4 v130, s[34:35]
	s_nop 0
	s_add_i32 m0, s36, 0x2000
	s_nop 0
	global_load_lds_dwordx4 v132, s[34:35]
	s_nop 0
	s_mov_b32 m0, s49
	s_nop 0
	global_load_lds_dwordx4 v130, s[84:85]
	s_nop 0
	s_mov_b32 m0, s50
	s_nop 0
	global_load_lds_dwordx4 v132, s[84:85]
	s_waitcnt vmcnt(8)
	s_waitcnt lgkmcnt(0)
	s_barrier
	s_waitcnt lgkmcnt(0)
	v_mfma_f32_16x16x32_bf16 v[62:65], v[142:145], v[184:187], v[62:65]
	v_mfma_f32_16x16x32_bf16 v[58:61], v[158:161], v[184:187], v[58:61]
	v_mfma_f32_16x16x32_bf16 v[50:53], v[142:145], v[192:195], v[50:53]
	v_mfma_f32_16x16x32_bf16 v[42:45], v[158:161], v[192:195], v[42:45]
	v_mfma_f32_16x16x32_bf16 v[34:37], v[142:145], v[200:203], v[34:37]
	v_mfma_f32_16x16x32_bf16 v[26:29], v[158:161], v[200:203], v[26:29]
	v_mfma_f32_16x16x32_bf16 v[14:17], v[142:145], v[208:211], v[14:17]
	v_mfma_f32_16x16x32_bf16 v[10:13], v[158:161], v[208:211], v[10:13]
	v_mfma_f32_16x16x32_bf16 v[62:65], v[154:157], v[188:191], v[62:65]
	v_mfma_f32_16x16x32_bf16 v[58:61], v[162:165], v[188:191], v[58:61]
	v_mfma_f32_16x16x32_bf16 v[50:53], v[154:157], v[196:199], v[50:53]
	v_mfma_f32_16x16x32_bf16 v[42:45], v[162:165], v[196:199], v[42:45]
	v_mfma_f32_16x16x32_bf16 v[34:37], v[154:157], v[204:207], v[34:37]
	v_mfma_f32_16x16x32_bf16 v[26:29], v[162:165], v[204:207], v[26:29]
	v_mfma_f32_16x16x32_bf16 v[14:17], v[154:157], v[212:215], v[14:17]
	v_mfma_f32_16x16x32_bf16 v[10:13], v[162:165], v[212:215], v[10:13]
	v_mfma_f32_16x16x32_bf16 v[54:57], v[166:169], v[184:187], v[54:57]
	v_mfma_f32_16x16x32_bf16 v[46:49], v[174:177], v[184:187], v[46:49]
	v_mfma_f32_16x16x32_bf16 v[38:41], v[166:169], v[192:195], v[38:41]
	v_mfma_f32_16x16x32_bf16 v[30:33], v[174:177], v[192:195], v[30:33]
	v_mfma_f32_16x16x32_bf16 v[22:25], v[166:169], v[200:203], v[22:25]
	v_mfma_f32_16x16x32_bf16 v[18:21], v[174:177], v[200:203], v[18:21]
	v_mfma_f32_16x16x32_bf16 v[6:9], v[166:169], v[208:211], v[6:9]
	v_mfma_f32_16x16x32_bf16 v[2:5], v[174:177], v[208:211], v[2:5]
	v_mfma_f32_16x16x32_bf16 v[54:57], v[170:173], v[188:191], v[54:57]
	v_mfma_f32_16x16x32_bf16 v[46:49], v[178:181], v[188:191], v[46:49]
	v_mfma_f32_16x16x32_bf16 v[38:41], v[170:173], v[196:199], v[38:41]
	v_mfma_f32_16x16x32_bf16 v[30:33], v[178:181], v[196:199], v[30:33]
	v_mfma_f32_16x16x32_bf16 v[22:25], v[170:173], v[204:207], v[22:25]
	v_mfma_f32_16x16x32_bf16 v[18:21], v[178:181], v[204:207], v[18:21]
	v_mfma_f32_16x16x32_bf16 v[6:9], v[170:173], v[212:215], v[6:9]
	v_mfma_f32_16x16x32_bf16 v[2:5], v[178:181], v[212:215], v[2:5]
	s_barrier
	s_add_i32 s61, s61, 2
	s_add_u32 s30, s30, 0x100
	s_addc_u32 s31, s31, 0
	s_add_u32 s59, s59, 0x100
	s_addc_u32 s60, s60, 0
	s_cmp_gt_u32 s61, 61
	s_cbranch_scc0 .LBB0_707
	s_and_b64 vcc, exec, s[14:15]
	s_cbranch_vccz .LBB0_710
	s_barrier
